# dsa attention: straight-line bias+mask path for tiles far from the diagonal
# speedup vs baseline: 1.0177x; 1.0017x over previous
.Ldsa_far:
	s_nop 2
	v_fma_f32 v205, v84, v153, v203
	v_fma_f32 v206, v68, v153, v203
	v_bfe_i32 v68, v158, v149, 1
	v_bfe_i32 v182, v159, v149, 1
	v_bitop3_b32 v84, v205, v229, v68 bitop3:0xe4
	v_bitop3_b32 v68, v206, v229, v182 bitop3:0xe4
	v_max3_f32 v204, v229, v84, v68
	v_fma_f32 v208, v85, v153, v203
	v_fma_f32 v209, v69, v153, v203
	v_bfe_i32 v69, v158, v172, 1
	v_bfe_i32 v210, v159, v172, 1
	v_bitop3_b32 v85, v208, v229, v69 bitop3:0xe4
	v_bitop3_b32 v69, v209, v229, v210 bitop3:0xe4
	v_max3_f32 v204, v204, v85, v69
	v_fma_f32 v205, v86, v153, v203
	v_fma_f32 v206, v70, v153, v203
	v_bfe_i32 v70, v158, v173, 1
	v_bfe_i32 v182, v159, v173, 1
	v_bitop3_b32 v86, v205, v229, v70 bitop3:0xe4
	v_bitop3_b32 v70, v206, v229, v182 bitop3:0xe4
	v_max3_f32 v204, v204, v86, v70
	v_fma_f32 v208, v87, v153, v203
	v_fma_f32 v209, v71, v153, v203
	v_bfe_i32 v71, v158, v174, 1
	v_bfe_i32 v210, v159, v174, 1
	v_bitop3_b32 v87, v208, v229, v71 bitop3:0xe4
	v_bitop3_b32 v71, v209, v229, v210 bitop3:0xe4
	v_max3_f32 v204, v204, v87, v71
	v_fma_f32 v205, v88, v153, v203
	v_fma_f32 v206, v72, v153, v203
	v_bfe_i32 v72, v158, v175, 1
	v_bfe_i32 v182, v159, v175, 1
	v_bitop3_b32 v88, v205, v229, v72 bitop3:0xe4
	v_bitop3_b32 v72, v206, v229, v182 bitop3:0xe4
	v_max3_f32 v204, v204, v88, v72
	v_fma_f32 v208, v89, v153, v203
	v_fma_f32 v209, v73, v153, v203
	v_bfe_i32 v73, v158, v176, 1
	v_bfe_i32 v210, v159, v176, 1
	v_bitop3_b32 v89, v208, v229, v73 bitop3:0xe4
	v_bitop3_b32 v73, v209, v229, v210 bitop3:0xe4
	v_max3_f32 v204, v204, v89, v73
	v_fma_f32 v205, v90, v153, v203
	v_fma_f32 v206, v74, v153, v203
	v_bfe_i32 v74, v158, v177, 1
	v_bfe_i32 v182, v159, v177, 1
	v_bitop3_b32 v90, v205, v229, v74 bitop3:0xe4
	v_bitop3_b32 v74, v206, v229, v182 bitop3:0xe4
	v_max3_f32 v204, v204, v90, v74
	v_fma_f32 v208, v91, v153, v203
	v_fma_f32 v209, v75, v153, v203
	v_bfe_i32 v75, v158, v178, 1
	v_bfe_i32 v210, v159, v178, 1
	v_bitop3_b32 v91, v208, v229, v75 bitop3:0xe4
	v_bitop3_b32 v75, v209, v229, v210 bitop3:0xe4
	v_max3_f32 v204, v204, v91, v75
	v_fma_f32 v205, v92, v153, v203
	v_fma_f32 v206, v76, v153, v203
	v_bfe_i32 v76, v158, v179, 1
	v_bfe_i32 v182, v159, v179, 1
	v_bitop3_b32 v92, v205, v229, v76 bitop3:0xe4
	v_bitop3_b32 v76, v206, v229, v182 bitop3:0xe4
	v_max3_f32 v204, v204, v92, v76
	v_fma_f32 v208, v93, v153, v203
	v_fma_f32 v209, v77, v153, v203
	v_bfe_i32 v77, v158, v180, 1
	v_bfe_i32 v210, v159, v180, 1
	v_bitop3_b32 v93, v208, v229, v77 bitop3:0xe4
	v_bitop3_b32 v77, v209, v229, v210 bitop3:0xe4
	v_max3_f32 v204, v204, v93, v77
	v_fma_f32 v205, v94, v153, v203
	v_fma_f32 v206, v78, v153, v203
	v_bfe_i32 v78, v158, v181, 1
	v_bfe_i32 v182, v159, v181, 1
	v_bitop3_b32 v94, v205, v229, v78 bitop3:0xe4
	v_bitop3_b32 v78, v206, v229, v182 bitop3:0xe4
	v_max3_f32 v204, v204, v94, v78
	v_fma_f32 v208, v95, v153, v203
	v_fma_f32 v209, v79, v153, v203
	v_bfe_i32 v79, v158, v194, 1
	v_bfe_i32 v210, v159, v194, 1
	v_bitop3_b32 v95, v208, v229, v79 bitop3:0xe4
	v_bitop3_b32 v79, v209, v229, v210 bitop3:0xe4
	v_max3_f32 v204, v204, v95, v79
	v_fma_f32 v205, v96, v153, v203
	v_fma_f32 v206, v80, v153, v203
	v_bfe_i32 v80, v158, v195, 1
	v_bfe_i32 v182, v159, v195, 1
	v_bitop3_b32 v96, v205, v229, v80 bitop3:0xe4
	v_bitop3_b32 v80, v206, v229, v182 bitop3:0xe4
	v_max3_f32 v204, v204, v96, v80
	v_fma_f32 v208, v97, v153, v203
	v_fma_f32 v209, v81, v153, v203
	v_bfe_i32 v81, v158, v196, 1
	v_bfe_i32 v210, v159, v196, 1
	v_bitop3_b32 v97, v208, v229, v81 bitop3:0xe4
	v_bitop3_b32 v81, v209, v229, v210 bitop3:0xe4
	v_max3_f32 v204, v204, v97, v81
	v_fma_f32 v205, v98, v153, v203
	v_fma_f32 v206, v82, v153, v203
	v_bfe_i32 v82, v158, v197, 1
	v_bfe_i32 v182, v159, v197, 1
	v_bitop3_b32 v98, v205, v229, v82 bitop3:0xe4
	v_bitop3_b32 v82, v206, v229, v182 bitop3:0xe4
	v_max3_f32 v204, v204, v98, v82
